# v58 + attention barrier phase shift applied to the PRIORITISED half (waves 0-3 take the tile barrier before their softmax scaling section)
# speedup vs baseline: 1.0053x; 1.0003x over previous
.LBB0_1343:
	s_and_b32 s3, s21, 3
	s_and_b64 s[4:5], exec, s[34:35]
	s_cselect_b32 s3, -1, s3
	s_cmp_eq_u32 s3, 2
	s_movk_i32 s4, 0x3080
	s_cselect_b32 s4, 0x2000, s4
	s_cmp_lg_u32 s3, 1
	s_cselect_b32 s4, s4, 0x1000
	s_cmp_gt_i32 s3, 0
	s_cselect_b32 s8, s4, 0
	s_mul_i32 s18, s8, 0xe00
	v_readlane_b32 s4, v253, 7
	v_readlane_b32 s5, v253, 8
	s_add_u32 s4, s4, s18
	v_lshlrev_b32_e32 v2, 8, v181
	v_mov_b32_e32 v3, v99
	v_lshl_add_u32 v7, v7, 7, v14
	s_addc_u32 s5, s5, 0
	v_lshlrev_b64 v[50:51], 1, v[2:3]
	v_cvt_pk_bf16_f32 v5, v5, v99
	ds_write_b16 v7, v5
	v_cvt_pk_bf16_f32 v4, v4, v99
	v_lshl_add_u64 v[2:3], s[4:5], 0, v[50:51]
	ds_write_b16 v7, v4 offset:32
	v_ashrrev_i32_e32 v4, 4, v6
	v_lshlrev_b32_e32 v5, 3, v6
	s_movk_i32 s4, 0x700
	v_and_b32_e32 v7, 0x78, v5
	v_mul_lo_u32 v8, v4, s4
	v_or_b32_e32 v8, v8, v7
	v_lshlrev_b32_e32 v52, 1, v8
	v_readfirstlane_b32 s4, v2
	v_readfirstlane_b32 s5, v3
	s_waitcnt lgkmcnt(0)
	s_barrier
	v_add_u32_e32 v54, 0x1c000, v52
	s_nop 1
	global_load_dwordx4 v[8:11], v52, s[4:5] offset:1792
	global_load_dwordx4 v[14:17], v54, s[4:5] offset:1792
	s_lshl_b32 s22, s8, 7
	v_readlane_b32 s8, v253, 5
	v_lshlrev_b32_e32 v26, 4, v6
	v_readlane_b32 s9, v253, 6
	s_add_u32 s24, s8, s22
	v_ashrrev_i32_e32 v13, 3, v6
	v_and_b32_e32 v30, 0x70, v26
	s_addc_u32 s25, s9, 0
	v_lshl_or_b32 v56, v13, 7, v30
	global_load_dwordx4 v[18:21], v52, s[4:5] offset:1536
	global_load_dwordx4 v[22:25], v54, s[4:5] offset:1536
	global_load_dwordx4 v[26:29], v56, s[24:25]
	v_lshlrev_b32_e32 v31, 7, v194
	v_lshlrev_b32_e32 v12, 1, v12
	v_readlane_b32 s4, v255, 34
	v_lshlrev_b32_e32 v32, 1, v4
	v_lshrrev_b32_e32 v33, 1, v4
	v_add3_u32 v12, s4, v31, v12
	v_and_b32_e32 v31, 0xfffff0, v4
	v_and_b32_e32 v35, 3, v4
	v_add_u32_e32 v36, 32, v4
	s_add_i32 s4, 0, 0x14000
	ds_read_b128 v[144:147], v12
	ds_read_b128 v[140:143], v12 offset:32
	ds_read_b128 v[136:139], v12 offset:64
	ds_read_b128 v[132:135], v12 offset:96
	v_and_or_b32 v12, v32, 8, v31
	v_and_or_b32 v31, v33, 4, v35
	v_and_b32_e32 v32, 0xfffff0, v36
	v_lshlrev_b32_e32 v33, 1, v36
	s_and_b64 s[0:1], s[0:1], exec
	v_bfe_u32 v34, v5, 5, 2
	v_lshrrev_b32_e32 v12, 1, v12
	v_and_or_b32 v32, v33, 8, v32
	s_cselect_b32 s5, 0x104, 4
	s_cmp_lt_u32 s3, 2
	v_lshlrev_b32_e32 v7, 1, v7
	v_or_b32_e32 v12, v12, v34
	v_lshrrev_b32_e32 v32, 1, v32
	s_cselect_b32 s3, 64, 0x42
	s_and_b64 s[0:1], exec, s[34:35]
	v_lshlrev_b32_e32 v31, 6, v31
	v_and_b32_e32 v35, 48, v7
	v_lshlrev_b32_e32 v12, 9, v12
	v_or_b32_e32 v32, v32, v34
	s_cselect_b32 s3, s5, s3
	s_add_i32 s0, 0, 0x8000
	v_lshlrev_b32_e32 v32, 9, v32
	v_or3_b32 v12, v12, v31, v35
	s_cmp_lg_u32 s0, -1
	v_or3_b32 v31, v32, v31, v35
	v_add_u32_e32 v205, 0, v12
	s_cselect_b32 s0, s0, 0
	s_movk_i32 s8, 0x70
	v_add_u32_e32 v206, 0, v31
	s_waitcnt vmcnt(0)
	v_mov_b32_e32 v12, s0
	s_movk_i32 s0, 0x180
	v_mul_lo_u32 v4, v4, s0
	v_bitop3_b32 v37, v98, v5, s8 bitop3:0x78
	s_waitcnt vmcnt(4)
	ds_write_b128 v205, v[8:11]
	s_waitcnt vmcnt(3)
	ds_write_b128 v206, v[14:17]
	v_lshrrev_b32_e32 v8, 1, v6
	v_bitop3_b32 v7, v7, v8, s8 bitop3:0x78
	v_add3_u32 v207, v7, v4, 0
	v_mul_lo_u32 v4, v13, s0
	v_or_b32_e32 v7, 0x100, v30
	v_and_b32_e32 v8, 0x70, v6
	v_mad_u32_u24 v53, v195, s0, v12
	v_xad_u32 v4, v7, v8, v4
	v_add_u32_e32 v201, v37, v53
	v_add_u32_e32 v208, 0, v4
	s_waitcnt vmcnt(2)
	ds_write_b128 v207, v[18:21] offset:32768
	s_waitcnt vmcnt(1)
	ds_write_b128 v207, v[22:25] offset:45056
	s_waitcnt vmcnt(0)
	ds_write_b128 v208, v[26:29] offset:32768
	s_waitcnt lgkmcnt(0)
	s_barrier
	ds_read_b128 v[8:11], v201
	ds_read_b128 v[12:15], v201 offset:128
	s_waitcnt lgkmcnt(1)
	v_mfma_f32_32x32x16_bf16 v[18:33], v[8:11], v[128:131], 0
	ds_read_b128 v[8:11], v201 offset:12288
	ds_read_b128 v[60:63], v201 offset:256
	v_and_b32_e32 v4, 0x70, v5
	v_bitop3_b32 v5, v98, v4, 32 bitop3:0x36
	v_add_u32_e32 v203, v5, v53
	v_bitop3_b32 v5, v98, v4, 64 bitop3:0x36
	v_add_u32_e32 v204, v5, v53
	s_waitcnt lgkmcnt(1)
	v_mfma_f32_32x32x16_bf16 v[34:49], v[8:11], v[128:131], 0
	ds_read_b128 v[8:11], v203
	ds_read_b128 v[64:67], v203 offset:128
	ds_read_b128 v[68:71], v203 offset:256
	s_movk_i32 s0, 0x60
	v_bitop3_b32 v4, v98, v4, s0 bitop3:0x36
	v_add_u32_e32 v202, v4, v53
	s_mov_b64 s[0:1], 0x38700
	v_lshl_add_u64 v[4:5], v[2:3], 0, s[0:1]
	s_waitcnt lgkmcnt(2)
	v_mfma_f32_32x32x16_bf16 v[18:33], v[8:11], v[124:127], v[18:33]
	ds_read_b128 v[8:11], v203 offset:12288
	s_mov_b64 s[0:1], 0x38600
	v_lshl_add_u64 v[2:3], v[2:3], 0, s[0:1]
	v_readfirstlane_b32 s0, v4
	v_readfirstlane_b32 s1, v5
	v_readfirstlane_b32 s8, v2
	v_readfirstlane_b32 s9, v3
	s_waitcnt lgkmcnt(0)
	v_mfma_f32_32x32x16_bf16 v[34:49], v[8:11], v[124:127], v[34:49]
	ds_read_b128 v[8:11], v204
	ds_read_b128 v[72:75], v204 offset:128
	ds_read_b128 v[76:79], v204 offset:256
	v_mov_b32_e32 v57, v99
	v_add_u32_e32 v209, 0x3000, v207
	s_cmp_lg_u32 0, -1
	v_lshlrev_b32_e32 v4, 1, v58
	v_and_b32_e32 v4, 32, v4
	s_waitcnt lgkmcnt(2)
	v_mfma_f32_32x32x16_bf16 v[18:33], v[8:11], v[120:123], v[18:33]
	ds_read_b128 v[8:11], v204 offset:12288
	s_mov_b32 s36, s63
	s_mov_b32 s37, s63
	s_mov_b32 s19, s63
	s_mov_b32 s38, s63
	s_mov_b32 s39, s63
	s_mov_b32 s40, s63
	s_waitcnt lgkmcnt(0)
	v_mfma_f32_32x32x16_bf16 v[34:49], v[8:11], v[120:123], v[34:49]
	ds_read_b128 v[8:11], v202
	ds_read_b128 v[80:83], v202 offset:128
	s_mov_b32 s41, s63
	s_mov_b32 s42, s63
	s_mov_b32 s43, s63
	s_mov_b32 s44, s63
	s_mov_b32 s45, s63
	s_mov_b32 s46, s63
	s_waitcnt lgkmcnt(1)
	v_mfma_f32_32x32x16_bf16 v[18:33], v[8:11], v[116:119], v[18:33]
	ds_read_b128 v[8:11], v202 offset:12288
	ds_read_b128 v[84:87], v202 offset:256
	s_mov_b32 s47, s63
	s_mov_b32 s48, s63
	s_mov_b32 s49, s63
	s_mov_b32 s50, s63
	s_mov_b32 s51, s63
	s_mov_b32 s23, s63
	v_mfma_f32_32x32x16_bf16 v[18:33], v[12:15], v[112:115], v[18:33]
	v_mov_b32_e32 v53, v99
	v_mov_b32_e32 v55, v99
	v_lshl_add_u64 v[182:183], s[22:23], 0, v[56:57]
	v_mov_b32_e32 v227, 0x3200
	v_mov_b32_e32 v199, 0
	s_waitcnt lgkmcnt(1)
	v_mfma_f32_32x32x16_bf16 v[34:49], v[8:11], v[116:119], v[34:49]
	ds_read_b128 v[8:11], v201 offset:12416
	ds_read_b128 v[12:15], v201 offset:12544
	v_mfma_f32_32x32x16_bf16 v[18:33], v[64:67], v[108:111], v[18:33]
	s_waitcnt lgkmcnt(1)
	v_mfma_f32_32x32x16_bf16 v[34:49], v[8:11], v[112:115], v[34:49]
	ds_read_b128 v[8:11], v203 offset:12416
	ds_read_b128 v[64:67], v203 offset:12544
	v_mfma_f32_32x32x16_bf16 v[18:33], v[72:75], v[104:107], v[18:33]
	s_waitcnt lgkmcnt(1)
	v_mfma_f32_32x32x16_bf16 v[34:49], v[8:11], v[108:111], v[34:49]
	ds_read_b128 v[8:11], v204 offset:12416
	ds_read_b128 v[72:75], v204 offset:12544
	v_mfma_f32_32x32x16_bf16 v[18:33], v[80:83], v[100:103], v[18:33]
	s_waitcnt lgkmcnt(1)
	v_mfma_f32_32x32x16_bf16 v[34:49], v[8:11], v[104:107], v[34:49]
	ds_read_b128 v[8:11], v202 offset:12416
	ds_read_b128 v[80:83], v202 offset:12544
	v_mfma_f32_32x32x16_bf16 v[18:33], v[60:63], v[144:147], v[18:33]
	global_load_dwordx4 v[60:63], v54, s[0:1]
	global_load_dwordx4 v[88:91], v52, s[8:9]
	global_load_dwordx4 v[92:95], v52, s[0:1]
	global_load_dwordx4 v[148:151], v54, s[8:9]
	s_movk_i32 s0, 0x2000
	s_mov_b32 s8, 2
	s_waitcnt lgkmcnt(1)
	v_mfma_f32_32x32x16_bf16 v[34:49], v[8:11], v[100:103], v[34:49]
	v_lshl_add_u64 v[8:9], s[24:25], 0, v[56:57]
	v_add_co_u32_e32 v2, vcc, s0, v8
	v_cmp_gt_u32_e64 s[0:1], 32, v58
	s_nop 0
	v_addc_co_u32_e32 v3, vcc, 0, v9, vcc
	global_load_dwordx4 v[152:155], v[2:3], off
	v_mfma_f32_32x32x16_bf16 v[18:33], v[68:71], v[140:143], v[18:33]
	s_waitcnt vmcnt(0)
	s_waitcnt vmcnt(2)
	ds_write_b128 v205, v[92:95] offset:16384
	ds_write_b128 v206, v[60:63] offset:16384
	ds_write_b128 v207, v[88:91] offset:57344
	s_waitcnt vmcnt(1)
	ds_write_b128 v209, v[148:151] offset:57344
	s_waitcnt vmcnt(0)
	ds_write_b128 v208, v[152:155] offset:57344
	v_mfma_f32_32x32x16_bf16 v[34:49], v[12:15], v[144:147], v[34:49]
	v_and_b32_e32 v2, 0x3fffffc0, v6
	v_lshl_add_u32 v196, v2, 2, s4
	s_cselect_b32 s4, 0, 0
	v_lshlrev_b32_e32 v3, 4, v58
	v_lshlrev_b32_e32 v2, 3, v58
	v_and_b32_e32 v3, 0xc0, v3
	v_and_or_b32 v3, v2, 24, v3
	v_mfma_f32_32x32x16_bf16 v[18:33], v[76:79], v[136:139], v[18:33]
	v_and_b32_e32 v2, 0x100, v2
	v_or3_b32 v59, v3, v4, v2
	v_mov_b64_e32 v[2:3], s[36:37]
	v_add_u32_e32 v200, s4, v59
	v_mov_b64_e32 v[16:17], s[50:51]
	v_mov_b64_e32 v[4:5], s[38:39]
	v_mov_b64_e32 v[6:7], s[40:41]
	v_mfma_f32_32x32x16_bf16 v[34:49], v[64:67], v[140:143], v[34:49]
	v_mov_b64_e32 v[8:9], s[42:43]
	v_mov_b64_e32 v[10:11], s[44:45]
	v_mov_b64_e32 v[12:13], s[46:47]
	v_mov_b64_e32 v[14:15], s[48:49]
	v_lshl_add_u32 v197, v195, 2, v196
	s_waitcnt lgkmcnt(0)
	s_barrier
	v_mfma_f32_32x32x16_bf16 v[18:33], v[84:87], v[132:135], v[18:33]
	v_mfma_f32_32x32x16_bf16 v[34:49], v[72:75], v[136:139], v[34:49]
	s_nop 10
	v_max_f32_e32 v64, v19, v19
	v_max_f32_e32 v65, v18, v18
	v_max_f32_e32 v64, v65, v64
	v_max3_f32 v64, v64, v20, v21
	v_max3_f32 v64, v64, v22, v23
	v_max3_f32 v64, v64, v24, v25
	v_max3_f32 v64, v64, v26, v27
	v_mfma_f32_32x32x16_bf16 v[34:49], v[80:83], v[132:135], v[34:49]
	v_max3_f32 v64, v64, v28, v29
	v_max3_f32 v64, v64, v30, v31
	v_max3_f32 v64, v64, v32, v33
	s_nop 8
	v_max3_f32 v64, v64, v34, v35
	v_max3_f32 v64, v64, v36, v37
	v_max3_f32 v64, v64, v38, v39
	v_max3_f32 v64, v64, v40, v41
	v_max3_f32 v64, v64, v42, v43
	v_max3_f32 v64, v64, v44, v45
	v_max3_f32 v64, v64, v46, v47
	v_max3_f32 v64, v64, v48, v49
	v_mov_b32_e32 v65, v64
	s_nop 1
	v_permlane32_swap_b32_e32 v64, v65
	v_max_f32_e32 v65, v65, v65
	v_max_f32_e32 v64, v64, v64
	v_max_f32_e32 v64, v64, v65
	v_max_f32_e32 v60, 0xf149f2ca, v64
	v_sub_f32_e32 v61, 0xf149f2ca, v60
	v_mul_f32_e32 v61, 0x3dd53b94, v61
	v_add_f32_e32 v65, 0x7149f2ca, v64
	v_exp_f32_e32 v61, v61
	v_cmp_ge_f32_e32 vcc, s11, v65
	s_cmp_eq_u64 vcc, exec
	s_cselect_b64 vcc, -1, 0
	v_cndmask_b32_e64 v210, v61, 1.0, vcc
	v_mov_b32_e32 v61, 0xf149f2ca
	v_cndmask_b32_e32 v211, v60, v61, vcc
	v_mul_f32_e32 v60, 0xbdd53b94, v211
	v_fmamk_f32 v18, v18, 0x3dd53b94, v60
	v_exp_f32_e32 v169, v18
	v_fmamk_f32 v18, v19, 0x3dd53b94, v60
	v_exp_f32_e32 v191, v18
	v_fmamk_f32 v18, v20, 0x3dd53b94, v60
	v_exp_f32_e32 v170, v18
	v_fmamk_f32 v18, v21, 0x3dd53b94, v60
	v_exp_f32_e32 v192, v18
	v_fmamk_f32 v18, v22, 0x3dd53b94, v60
	v_exp_f32_e32 v190, v18
	v_fmamk_f32 v18, v23, 0x3dd53b94, v60
	v_exp_f32_e32 v193, v18
	v_fmamk_f32 v18, v24, 0x3dd53b94, v60
	v_exp_f32_e32 v171, v18
	v_fmamk_f32 v18, v25, 0x3dd53b94, v60
	v_exp_f32_e32 v189, v18
	v_fmamk_f32 v18, v26, 0x3dd53b94, v60
	v_exp_f32_e32 v173, v18
	v_fmamk_f32 v18, v27, 0x3dd53b94, v60
	v_exp_f32_e32 v175, v18
	v_fmamk_f32 v18, v28, 0x3dd53b94, v60
	v_exp_f32_e32 v174, v18
	v_fmamk_f32 v18, v29, 0x3dd53b94, v60
	v_exp_f32_e32 v188, v18
	v_fmamk_f32 v18, v30, 0x3dd53b94, v60
	v_exp_f32_e32 v164, v18
	v_fmamk_f32 v18, v31, 0x3dd53b94, v60
	v_pk_fma_f32 v[148:149], v[48:49], s[56:57], v[60:61] op_sel_hi:[1,0,0]
	v_pk_fma_f32 v[154:155], v[46:47], s[56:57], v[60:61] op_sel_hi:[1,0,0]
	v_pk_fma_f32 v[158:159], v[44:45], s[56:57], v[60:61] op_sel_hi:[1,0,0]
	v_pk_fma_f32 v[150:151], v[42:43], s[56:57], v[60:61] op_sel_hi:[1,0,0]
	v_pk_fma_f32 v[152:153], v[40:41], s[56:57], v[60:61] op_sel_hi:[1,0,0]
	v_pk_fma_f32 v[156:157], v[38:39], s[56:57], v[60:61] op_sel_hi:[1,0,0]
	v_pk_fma_f32 v[160:161], v[36:37], s[56:57], v[60:61] op_sel_hi:[1,0,0]
	v_pk_fma_f32 v[162:163], v[34:35], s[56:57], v[60:61] op_sel_hi:[1,0,0]
	v_exp_f32_e32 v166, v18
	v_fmamk_f32 v18, v32, 0x3dd53b94, v60
	v_fmac_f32_e32 v60, 0x3dd53b94, v33
	v_exp_f32_e32 v165, v18
	v_exp_f32_e32 v167, v60
	s_addk_i32 s4, 0x4000
	v_lshl_add_u64 v[18:19], s[18:19], 0, v[50:51]
	v_add_u32_e32 v198, s4, v59
	v_lshl_add_u64 v[184:185], v[18:19], 0, v[54:55]
	v_lshl_add_u64 v[186:187], v[18:19], 0, v[52:53]
	v_mov_b64_e32 v[64:65], v[16:17]
	v_mov_b64_e32 v[48:49], v[16:17]
	v_mov_b64_e32 v[32:33], v[16:17]
	v_mov_b64_e32 v[62:63], v[14:15]
	v_mov_b64_e32 v[60:61], v[12:13]
	v_mov_b64_e32 v[58:59], v[10:11]
	v_mov_b64_e32 v[56:57], v[8:9]
	v_mov_b64_e32 v[54:55], v[6:7]
	v_mov_b64_e32 v[52:53], v[4:5]
	v_mov_b64_e32 v[50:51], v[2:3]
	v_mov_b64_e32 v[46:47], v[14:15]
	v_mov_b64_e32 v[44:45], v[12:13]
	v_mov_b64_e32 v[42:43], v[10:11]
	v_mov_b64_e32 v[40:41], v[8:9]
	v_mov_b64_e32 v[38:39], v[6:7]
	v_mov_b64_e32 v[36:37], v[4:5]
	v_mov_b64_e32 v[34:35], v[2:3]
	v_mov_b64_e32 v[30:31], v[14:15]
	v_mov_b64_e32 v[28:29], v[12:13]
	v_mov_b64_e32 v[26:27], v[10:11]
	v_mov_b64_e32 v[24:25], v[8:9]
	v_mov_b64_e32 v[22:23], v[6:7]
	v_mov_b64_e32 v[20:21], v[4:5]
	v_mov_b64_e32 v[18:19], v[2:3]
	v_and_b32_e32 v230, 63, v0
	v_lshrrev_b32_e32 v231, 6, v0
	v_lshrrev_b32_e32 v232, 4, v0
	v_mul_u32_u24_e32 v232, 0xe00, v232
	v_and_b32_e32 v233, 15, v0
	v_lshl_add_u32 v232, v233, 4, v232
	v_sub_u32_e32 v232, v186, v232
	v_lshrrev_b32_e32 v233, 3, v0
	v_and_b32_e32 v236, 7, v0
	v_lshlrev_b32_e32 v236, 4, v236
	v_lshl_add_u32 v233, v233, 7, v236
	v_sub_u32_e32 v233, v182, v233
	v_add_u32_e32 v232, 0x39d1dc00, v232
	v_add_u32_e32 v233, 0x39b15600, v233
	v_mov_b32_e32 v243, 0
	v_mov_b32_e32 v244, 0x2000
	v_mov_b32_e32 v245, 0x38000
	v_bfe_u32 v236, v230, 2, 3
	v_lshl_add_u32 v236, v231, 3, v236
	v_and_b32_e32 v237, 0xfffffff3, v236
	v_and_b32_e32 v238, 4, v236
	v_lshl_or_b32 v237, v238, 1, v237
	v_and_b32_e32 v238, 8, v236
	v_lshrrev_b32_e32 v238, 1, v238
	v_or_b32_e32 v237, v237, v238
	v_add_u32_e32 v237, 64, v237
	v_mul_u32_u24_e32 v237, 0xe00, v237
	v_add_u32_e32 v237, v237, v232
	v_lshrrev_b32_e32 v238, 5, v230
	v_lshlrev_b32_e32 v238, 6, v238
	v_and_b32_e32 v239, 3, v230
	v_lshl_add_u32 v238, v239, 4, v238
	v_add_u32_e32 v237, v237, v238
	v_add_u32_e32 v242, 0x100, v237
	v_lshl_add_u64 v[206:207], s[14:15], 0, v[242:243]
	v_mov_b32_e32 v236, v230
	v_mul_u32_u24_e32 v237, 0x2ab, v236
	v_lshrrev_b32_e32 v237, 14, v237
	v_mul_u32_u24_e32 v238, 24, v237
	v_sub_u32_e32 v238, v236, v238
	v_lshl_add_u32 v237, v231, 3, v237
	v_bfe_u32 v239, v237, 1, 3
	v_xor_b32_e32 v238, v238, v239
	v_add_u32_e32 v237, 0x80, v237
	v_mul_u32_u24_e32 v240, 0xe00, v237
	v_add_u32_e32 v240, v240, v232
	v_lshl_add_u32 v240, v238, 4, v240
	v_lshl_add_u32 v241, v237, 7, v233
	v_lshl_add_u32 v241, v238, 4, v241
	v_subrev_u32_e32 v241, 0x100, v241
	v_cmp_gt_u32_e32 vcc, 16, v238
	s_nop 1
	v_cndmask_b32_e32 v242, v241, v240, vcc
	v_cndmask_b32_e32 v205, v244, v245, vcc
	v_lshl_add_u64 v[182:183], s[14:15], 0, v[242:243]
	v_add_u32_e32 v236, 0x40, v230
	v_mul_u32_u24_e32 v237, 0x2ab, v236
	v_lshrrev_b32_e32 v237, 14, v237
	v_mul_u32_u24_e32 v238, 24, v237
	v_sub_u32_e32 v238, v236, v238
	v_lshl_add_u32 v237, v231, 3, v237
	v_bfe_u32 v239, v237, 1, 3
	v_xor_b32_e32 v238, v238, v239
	v_add_u32_e32 v237, 0x80, v237
	v_mul_u32_u24_e32 v240, 0xe00, v237
	v_add_u32_e32 v240, v240, v232
	v_lshl_add_u32 v240, v238, 4, v240
	v_lshl_add_u32 v241, v237, 7, v233
	v_lshl_add_u32 v241, v238, 4, v241
	v_subrev_u32_e32 v241, 0x100, v241
	v_cmp_gt_u32_e32 vcc, 16, v238
	s_nop 1
	v_cndmask_b32_e32 v242, v241, v240, vcc
	v_cndmask_b32_e32 v208, v244, v245, vcc
	v_lshl_add_u64 v[184:185], s[14:15], 0, v[242:243]
	v_add_u32_e32 v236, 0x80, v230
	v_mul_u32_u24_e32 v237, 0x2ab, v236
	v_lshrrev_b32_e32 v237, 14, v237
	v_mul_u32_u24_e32 v238, 24, v237
	v_sub_u32_e32 v238, v236, v238
	v_lshl_add_u32 v237, v231, 3, v237
	v_bfe_u32 v239, v237, 1, 3
	v_xor_b32_e32 v238, v238, v239
	v_add_u32_e32 v237, 0x80, v237
	v_mul_u32_u24_e32 v240, 0xe00, v237
	v_add_u32_e32 v240, v240, v232
	v_lshl_add_u32 v240, v238, 4, v240
	v_lshl_add_u32 v241, v237, 7, v233
	v_lshl_add_u32 v241, v238, 4, v241
	v_subrev_u32_e32 v241, 0x100, v241
	v_cmp_gt_u32_e32 vcc, 16, v238
	s_nop 1
	v_cndmask_b32_e32 v242, v241, v240, vcc
	v_cndmask_b32_e32 v209, v244, v245, vcc
	v_lshl_add_u64 v[186:187], s[14:15], 0, v[242:243]
	v_lshrrev_b32_e32 v236, 8, v0
	s_nop 0
	v_readfirstlane_b32 s98, v236
	s_xor_b32 s98, s98, 1
